# sec 6.4: the VALU at the head of both attention compute segments (3 v_add / 3 v_exp) moved behind the first MFMA; on top of v58
# baseline (speedup 1.0000x reference)
.LBB0_1344:
	ds_read_b128 v[230:233], v203 offset:24576
	ds_read_b128 v[236:239], v203 offset:36864
	ds_read_b128 v[240:243], v204 offset:24576
	ds_read_b128 v[244:247], v204 offset:36864
	ds_read_b128 v[66:69], v201 offset:36864
	ds_read_b128 v[70:73], v201 offset:24576
	ds_read_b128 v[212:215], v202 offset:24576
	ds_read_b128 v[216:219], v202 offset:36864
	s_waitcnt lgkmcnt(2)
	v_mfma_f32_32x32x16_bf16 v[82:97], v[70:73], v[128:131], 0
	v_add_f32_e32 v168, 0, v169
	v_add_f32_e32 v168, v191, v168
	v_add_f32_e32 v168, v170, v168
	v_add_f32_e32 v168, v192, v168
	v_add_f32_e32 v168, v190, v168
	v_add_f32_e32 v168, v193, v168
	v_add_f32_e32 v168, v171, v168
	v_add_f32_e32 v168, v189, v168
	v_add_f32_e32 v168, v173, v168
	v_add_f32_e32 v168, v175, v168
	v_mfma_f32_32x32x16_bf16 v[66:81], v[66:69], v[128:131], 0
	v_add_f32_e32 v168, v174, v168
	v_add_f32_e32 v168, v188, v168
	v_exp_f32_e32 v162, v162
	v_add_f32_e32 v168, v164, v168
	v_exp_f32_e32 v163, v163
	v_add_f32_e32 v168, v166, v168
	v_exp_f32_e32 v160, v160
	v_mfma_f32_32x32x16_bf16 v[82:97], v[230:233], v[124:127], v[82:97]
	v_add_f32_e32 v168, v165, v168
	v_exp_f32_e32 v161, v161
	v_add_f32_e32 v168, v167, v168
	v_exp_f32_e32 v156, v156
	v_add_f32_e32 v168, v162, v168
	v_exp_f32_e32 v157, v157
	v_add_f32_e32 v168, v163, v168
	v_mfma_f32_32x32x16_bf16 v[66:81], v[236:239], v[124:127], v[66:81]
	ds_read_b128 v[230:233], v201 offset:24704
	ds_read_b128 v[236:239], v201 offset:36992
	v_exp_f32_e32 v152, v152
	v_add_f32_e32 v168, v160, v168
	v_exp_f32_e32 v153, v153
	v_add_f32_e32 v168, v161, v168
	v_exp_f32_e32 v150, v150
	v_add_f32_e32 v168, v156, v168
	v_mfma_f32_32x32x16_bf16 v[82:97], v[240:243], v[120:123], v[82:97]
	v_exp_f32_e32 v151, v151
	v_add_f32_e32 v168, v157, v168
	v_exp_f32_e32 v158, v158
	v_add_f32_e32 v168, v152, v168
	v_exp_f32_e32 v159, v159
	v_add_f32_e32 v168, v153, v168
	v_exp_f32_e32 v154, v154
	v_mfma_f32_32x32x16_bf16 v[66:81], v[244:247], v[120:123], v[66:81]
	ds_read_b128 v[240:243], v203 offset:24704
	ds_read_b128 v[244:247], v203 offset:36992
	v_add_f32_e32 v168, v150, v168
	v_exp_f32_e32 v155, v155
	v_add_f32_e32 v168, v151, v168
	v_exp_f32_e32 v148, v148
	v_add_f32_e32 v168, v158, v168
	v_exp_f32_e32 v149, v149
	s_waitcnt lgkmcnt(5)
	v_mfma_f32_32x32x16_bf16 v[82:97], v[212:215], v[116:119], v[82:97]
	v_add_f32_e32 v168, v159, v168
	v_add_f32_e32 v168, v154, v168
	v_add_f32_e32 v168, v155, v168
	v_add_f32_e32 v168, v148, v168
	s_waitcnt lgkmcnt(4)
	v_mfma_f32_32x32x16_bf16 v[66:81], v[216:219], v[116:119], v[66:81]
	ds_read_b128 v[212:215], v204 offset:24704
	ds_read_b128 v[216:219], v204 offset:36992
	s_waitcnt lgkmcnt(5)
	v_mfma_f32_32x32x16_bf16 v[82:97], v[230:233], v[112:115], v[82:97]
	s_waitcnt lgkmcnt(4)
	v_mfma_f32_32x32x16_bf16 v[66:81], v[236:239], v[112:115], v[66:81]
	ds_read_b128 v[230:233], v202 offset:24704
	ds_read_b128 v[236:239], v202 offset:36992
	s_waitcnt lgkmcnt(5)
	v_mfma_f32_32x32x16_bf16 v[82:97], v[240:243], v[108:111], v[82:97]
	s_waitcnt lgkmcnt(4)
	v_mfma_f32_32x32x16_bf16 v[66:81], v[244:247], v[108:111], v[66:81]
	ds_read_b128 v[240:243], v201 offset:24832
	ds_read_b128 v[244:247], v201 offset:37120
	s_waitcnt lgkmcnt(5)
	v_mfma_f32_32x32x16_bf16 v[82:97], v[212:215], v[104:107], v[82:97]
	s_waitcnt lgkmcnt(4)
	v_mfma_f32_32x32x16_bf16 v[66:81], v[216:219], v[104:107], v[66:81]
	ds_read_b128 v[212:215], v203 offset:24832
	ds_read_b128 v[216:219], v203 offset:37120
	s_waitcnt lgkmcnt(5)
	v_mfma_f32_32x32x16_bf16 v[82:97], v[230:233], v[100:103], v[82:97]
	s_waitcnt lgkmcnt(4)
	v_mfma_f32_32x32x16_bf16 v[66:81], v[236:239], v[100:103], v[66:81]
	ds_read_b128 v[230:233], v204 offset:24832
	ds_read_b128 v[236:239], v204 offset:37120
	s_waitcnt lgkmcnt(5)
	v_mfma_f32_32x32x16_bf16 v[82:97], v[240:243], v[144:147], v[82:97]
	s_waitcnt lgkmcnt(4)
	v_mfma_f32_32x32x16_bf16 v[66:81], v[244:247], v[144:147], v[66:81]
	ds_read_b128 v[240:243], v202 offset:24832
	ds_read_b128 v[244:247], v202 offset:37120
	s_waitcnt lgkmcnt(5)
	v_mfma_f32_32x32x16_bf16 v[82:97], v[212:215], v[140:143], v[82:97]
	v_add_f32_e32 v212, v149, v168
	v_mov_b32_e32 v213, v212
	v_cvt_pk_bf16_f32 v168, v169, v191
	v_cvt_pk_bf16_f32 v169, v170, v192
	v_cvt_pk_bf16_f32 v170, v190, v193
	v_cvt_pk_bf16_f32 v171, v171, v189
	v_cvt_pk_bf16_f32 v172, v173, v175
	s_waitcnt lgkmcnt(4)
	v_mfma_f32_32x32x16_bf16 v[66:81], v[216:219], v[140:143], v[66:81]
	v_cvt_pk_bf16_f32 v173, v174, v188
	v_cvt_pk_bf16_f32 v174, v164, v166
	v_permlane32_swap_b32_e32 v212, v213
	v_permlane32_swap_b32_e32 v168, v170
	v_cvt_pk_bf16_f32 v175, v165, v167
	s_waitcnt lgkmcnt(3)
	v_mfma_f32_32x32x16_bf16 v[82:97], v[230:233], v[136:139], v[82:97]
	v_permlane32_swap_b32_e32 v172, v174
	v_cvt_pk_bf16_f32 v214, v162, v163
	v_cvt_pk_bf16_f32 v215, v160, v161
	v_cvt_pk_bf16_f32 v216, v156, v157
	v_cvt_pk_bf16_f32 v217, v152, v153
	v_cvt_pk_bf16_f32 v230, v150, v151
	s_waitcnt lgkmcnt(2)
	v_mfma_f32_32x32x16_bf16 v[66:81], v[236:239], v[136:139], v[66:81]
	v_cvt_pk_bf16_f32 v231, v158, v159
	v_cvt_pk_bf16_f32 v232, v154, v155
	v_cvt_pk_bf16_f32 v233, v148, v149
	v_permlane32_swap_b32_e32 v169, v171
	v_permlane32_swap_b32_e32 v173, v175
	s_waitcnt lgkmcnt(1)
	v_mfma_f32_32x32x16_bf16 v[82:97], v[240:243], v[132:135], v[82:97]
	v_permlane32_swap_b32_e32 v214, v216
	v_permlane32_swap_b32_e32 v215, v217
	v_permlane32_swap_b32_e32 v230, v232
	v_permlane32_swap_b32_e32 v231, v233
	s_waitcnt lgkmcnt(0)
	v_mfma_f32_32x32x16_bf16 v[66:81], v[244:247], v[132:135], v[66:81]
	v_readfirstlane_b32 s4, v0
	s_nop 0
	s_lshl_b32 s5, s4, 4
	s_mul_i32 s4, s5, 3
	s_add_i32 m0, s4, 0x8000
	s_nop 0
	global_load_lds_dwordx4 v[182:183], off
	s_add_i32 m0, s4, 0x8400
	s_nop 0
	global_load_lds_dwordx4 v[184:185], off
	s_add_i32 m0, s4, 0x8800
	s_nop 0
	global_load_lds_dwordx4 v[186:187], off
	s_lshl_b32 s5, s5, 1
	s_add_i32 m0, s5, 0x4000
	s_nop 0
	global_load_lds_dwordx4 v[206:207], off
	s_add_i32 m0, s5, 0x4380
	s_nop 0
	global_load_lds_dwordx4 v[206:207], off offset:128
	v_add_co_u32_e32 v182, vcc, v182, v205
	s_nop 1
	v_addc_co_u32_e32 v183, vcc, 0, v183, vcc
	v_add_co_u32_e32 v184, vcc, v184, v208
	s_nop 1
	v_addc_co_u32_e32 v185, vcc, 0, v185, vcc
	v_add_co_u32_e32 v186, vcc, v186, v209
	s_nop 1
	v_addc_co_u32_e32 v187, vcc, 0, v187, vcc
	v_add_co_u32_e32 v206, vcc, 0x38000, v206
	s_nop 1
	v_addc_co_u32_e32 v207, vcc, 0, v207, vcc
	ds_read_b64_tr_b16 v[236:237], v200 offset:0
	ds_read_b64_tr_b16 v[238:239], v200 offset:0x800
	ds_read_b64_tr_b16 v[240:241], v200 offset:0x1000
	ds_read_b64_tr_b16 v[242:243], v200 offset:0x1800
	ds_read_b64_tr_b16 v[244:245], v200 offset:0x2000
	ds_read_b64_tr_b16 v[246:247], v200 offset:0x2800
	ds_read_b64_tr_b16 v[222:223], v200 offset:0x3000
	ds_read_b64_tr_b16 v[224:225], v200 offset:0x3800
	s_waitcnt lgkmcnt(0)
	s_nop 0
	v_mfma_f32_32x32x16_bf16 v[2:17], v[168:171], v[236:239], v[2:17]
	v_mfma_f32_32x32x16_bf16 v[2:17], v[172:175], v[240:243], v[2:17]
	v_mfma_f32_32x32x16_bf16 v[2:17], v[214:217], v[244:247], v[2:17]
	v_mfma_f32_32x32x16_bf16 v[2:17], v[230:233], v[222:225], v[2:17]
	ds_read_b64_tr_b16 v[222:223], v200 offset:0x200
	ds_read_b64_tr_b16 v[224:225], v200 offset:0xa00
	ds_read_b64_tr_b16 v[236:237], v200 offset:0x1200
	ds_read_b64_tr_b16 v[238:239], v200 offset:0x1a00
	ds_read_b64_tr_b16 v[240:241], v200 offset:0x2200
	ds_read_b64_tr_b16 v[242:243], v200 offset:0x2a00
	ds_read_b64_tr_b16 v[244:245], v200 offset:0x3200
	ds_read_b64_tr_b16 v[246:247], v200 offset:0x3a00
	s_waitcnt lgkmcnt(0)
	s_nop 0
	v_mfma_f32_32x32x16_bf16 v[50:65], v[168:171], v[222:225], v[50:65]
	ds_read_b64_tr_b16 v[222:223], v200 offset:0x400
	ds_read_b64_tr_b16 v[224:225], v200 offset:0xc00
	v_mfma_f32_32x32x16_bf16 v[50:65], v[172:175], v[236:239], v[50:65]
	ds_read_b64_tr_b16 v[236:237], v200 offset:0x1400
	ds_read_b64_tr_b16 v[238:239], v200 offset:0x1c00
	v_mfma_f32_32x32x16_bf16 v[50:65], v[214:217], v[240:243], v[50:65]
	ds_read_b64_tr_b16 v[240:241], v200 offset:0x2400
	ds_read_b64_tr_b16 v[242:243], v200 offset:0x2c00
	v_mfma_f32_32x32x16_bf16 v[50:65], v[230:233], v[244:247], v[50:65]
	ds_read_b64_tr_b16 v[244:245], v200 offset:0x3400
	ds_read_b64_tr_b16 v[246:247], v200 offset:0x3c00
	s_waitcnt lgkmcnt(0)
	v_mfma_f32_32x32x16_bf16 v[34:49], v[168:171], v[222:225], v[34:49]
	ds_read_b64_tr_b16 v[222:223], v200 offset:0x600
	ds_read_b64_tr_b16 v[224:225], v200 offset:0xe00
	v_mfma_f32_32x32x16_bf16 v[34:49], v[172:175], v[236:239], v[34:49]
	ds_read_b64_tr_b16 v[236:237], v200 offset:0x1600
	ds_read_b64_tr_b16 v[238:239], v200 offset:0x1e00
	v_mfma_f32_32x32x16_bf16 v[34:49], v[214:217], v[240:243], v[34:49]
	ds_read_b64_tr_b16 v[240:241], v200 offset:0x2600
	ds_read_b64_tr_b16 v[242:243], v200 offset:0x2e00
	v_mfma_f32_32x32x16_bf16 v[34:49], v[230:233], v[244:247], v[34:49]
	ds_read_b64_tr_b16 v[244:245], v200 offset:0x3600
	ds_read_b64_tr_b16 v[246:247], v200 offset:0x3e00
	s_waitcnt lgkmcnt(0)
	v_mfma_f32_32x32x16_bf16 v[18:33], v[168:171], v[222:225], v[18:33]
	v_max_f32_e32 v168, v83, v83
	v_max_f32_e32 v169, v82, v82
	v_max_f32_e32 v168, v169, v168
	v_max3_f32 v168, v168, v84, v85
	v_max3_f32 v168, v168, v86, v87
	v_max3_f32 v168, v168, v88, v89
	v_max3_f32 v168, v168, v90, v91
	v_max3_f32 v168, v168, v92, v93
	v_max3_f32 v168, v168, v94, v95
	v_mfma_f32_32x32x16_bf16 v[18:33], v[172:175], v[236:239], v[18:33]
	v_max3_f32 v168, v168, v96, v97
	v_max3_f32 v168, v168, v66, v67
	v_max3_f32 v168, v168, v68, v69
	v_max3_f32 v168, v168, v70, v71
	v_max3_f32 v168, v168, v72, v73
	v_max3_f32 v168, v168, v74, v75
	v_max3_f32 v168, v168, v76, v77
	v_max3_f32 v168, v168, v78, v79
	v_mfma_f32_32x32x16_bf16 v[18:33], v[214:217], v[240:243], v[18:33]
	v_max3_f32 v168, v168, v80, v81
	v_mov_b32_e32 v169, v168
	s_nop 1
	v_permlane32_swap_b32_e32 v168, v169
	v_max_f32_e32 v169, v169, v169
	v_max_f32_e32 v168, v168, v168
	v_max_f32_e32 v168, v168, v169
	v_sub_f32_e32 v169, v168, v211
	v_cmp_ge_f32_e32 vcc, s11, v169
	v_max_f32_e32 v169, v211, v211
	v_max_f32_e32 v168, v169, v168
	v_mfma_f32_32x32x16_bf16 v[18:33], v[230:233], v[244:247], v[18:33]
	v_sub_f32_e32 v169, v211, v168
	v_mul_f32_e32 v169, 0x3dd53b94, v169
	v_exp_f32_e32 v169, v169
	s_cmp_eq_u64 vcc, exec
	s_cselect_b64 s[18:19], -1, 0
	v_cndmask_b32_e64 v172, v169, 1.0, s[18:19]
	v_cmp_gt_f32_e32 vcc, 1.0, v172
	s_cbranch_vccz .LBB0_1348
	s_and_saveexec_b64 s[4:5], s[0:1]
	ds_write_b32 v197, v172 offset:128
	s_or_b64 exec, exec, s[4:5]
	s_waitcnt lgkmcnt(0)
	v_add_u32_e32 v160, v196, v98
	ds_read_b128 v[148:151], v160 offset:224
	ds_read_b128 v[152:155], v160 offset:192
	ds_read_b128 v[156:159], v160 offset:160
	ds_read_b128 v[160:163], v160 offset:128
	v_mov_b32_e32 v228, 0xffffce00
	s_waitcnt lgkmcnt(3)
	v_pk_mul_f32 v[14:15], v[14:15], v[148:149]
	s_waitcnt lgkmcnt(2)
	v_pk_mul_f32 v[10:11], v[10:11], v[152:153]
	s_waitcnt lgkmcnt(1)
	v_pk_mul_f32 v[6:7], v[6:7], v[156:157]
	v_pk_mul_f32 v[16:17], v[16:17], v[150:151]
	v_pk_mul_f32 v[12:13], v[12:13], v[154:155]
	v_pk_mul_f32 v[8:9], v[8:9], v[158:159]
	s_waitcnt lgkmcnt(0)
	v_pk_mul_f32 v[4:5], v[4:5], v[162:163]
	v_pk_mul_f32 v[2:3], v[2:3], v[160:161]
	v_pk_mul_f32 v[62:63], v[62:63], v[148:149]
	v_pk_mul_f32 v[58:59], v[58:59], v[152:153]
	v_pk_mul_f32 v[54:55], v[54:55], v[156:157]
	v_pk_mul_f32 v[64:65], v[64:65], v[150:151]
	v_pk_mul_f32 v[60:61], v[60:61], v[154:155]
	v_pk_mul_f32 v[56:57], v[56:57], v[158:159]
	v_pk_mul_f32 v[52:53], v[52:53], v[162:163]
	v_pk_mul_f32 v[50:51], v[50:51], v[160:161]
	v_pk_mul_f32 v[46:47], v[46:47], v[148:149]
	v_pk_mul_f32 v[42:43], v[42:43], v[152:153]
	v_pk_mul_f32 v[38:39], v[38:39], v[156:157]
	v_pk_mul_f32 v[48:49], v[48:49], v[150:151]
	v_pk_mul_f32 v[44:45], v[44:45], v[154:155]
	v_pk_mul_f32 v[40:41], v[40:41], v[158:159]
	v_pk_mul_f32 v[36:37], v[36:37], v[162:163]
	v_pk_mul_f32 v[34:35], v[34:35], v[160:161]
	v_pk_mul_f32 v[30:31], v[30:31], v[148:149]
	v_pk_mul_f32 v[26:27], v[26:27], v[152:153]
	v_pk_mul_f32 v[22:23], v[22:23], v[156:157]
	v_pk_mul_f32 v[32:33], v[32:33], v[150:151]
	v_pk_mul_f32 v[28:29], v[28:29], v[154:155]
	v_pk_mul_f32 v[24:25], v[24:25], v[158:159]
	v_pk_mul_f32 v[20:21], v[20:21], v[162:163]
	v_pk_mul_f32 v[18:19], v[18:19], v[160:161]
	s_branch .LBB0_1349

.LBB0_1349:
	v_cndmask_b32_e64 v173, v168, v211, s[18:19]
	v_mul_f32_e32 v164, 0xbdd53b94, v173
	v_fmamk_f32 v82, v82, 0x3dd53b94, v164
	v_fmamk_f32 v83, v83, 0x3dd53b94, v164
	v_fmamk_f32 v84, v84, 0x3dd53b94, v164
	v_fmamk_f32 v85, v85, 0x3dd53b94, v164
	v_fmamk_f32 v86, v86, 0x3dd53b94, v164
	v_fmamk_f32 v87, v87, 0x3dd53b94, v164
	v_fmamk_f32 v88, v88, 0x3dd53b94, v164
	v_fmamk_f32 v89, v89, 0x3dd53b94, v164
	v_fmamk_f32 v90, v90, 0x3dd53b94, v164
	v_fmamk_f32 v91, v91, 0x3dd53b94, v164
	v_fmamk_f32 v92, v92, 0x3dd53b94, v164
	v_fmamk_f32 v93, v93, 0x3dd53b94, v164
	v_fmamk_f32 v94, v94, 0x3dd53b94, v164
	v_fmamk_f32 v95, v95, 0x3dd53b94, v164
	v_fmamk_f32 v96, v96, 0x3dd53b94, v164
	v_fmamk_f32 v97, v97, 0x3dd53b94, v164
	v_fmamk_f32 v229, v68, 0x3dd53b94, v164
	v_fmamk_f32 v230, v69, 0x3dd53b94, v164
	v_fmamk_f32 v168, v73, 0x3dd53b94, v164
	v_fmamk_f32 v169, v74, 0x3dd53b94, v164
	v_fmamk_f32 v175, v66, 0x3dd53b94, v164
	v_fmamk_f32 v211, v67, 0x3dd53b94, v164
	v_fmamk_f32 v231, v70, 0x3dd53b94, v164
	v_fmamk_f32 v166, v71, 0x3dd53b94, v164
	v_fmamk_f32 v167, v72, 0x3dd53b94, v164
	v_fmamk_f32 v170, v75, 0x3dd53b94, v164
	v_fmamk_f32 v171, v76, 0x3dd53b94, v164
	v_fmamk_f32 v174, v77, 0x3dd53b94, v164
	v_fmamk_f32 v165, v78, 0x3dd53b94, v164
	v_exp_f32_e32 v161, v82
	v_exp_f32_e32 v163, v83
	v_exp_f32_e32 v159, v84
	v_exp_f32_e32 v162, v85
	v_exp_f32_e32 v158, v86
	v_exp_f32_e32 v160, v87
	v_exp_f32_e32 v156, v88
	v_exp_f32_e32 v157, v89
	v_exp_f32_e32 v153, v90
	v_exp_f32_e32 v155, v91
	v_exp_f32_e32 v152, v92
	v_exp_f32_e32 v154, v93
	v_exp_f32_e32 v149, v94
	v_exp_f32_e32 v151, v95
	v_exp_f32_e32 v148, v96
	v_exp_f32_e32 v150, v97
	v_fmamk_f32 v232, v79, 0x3dd53b94, v164
	v_fmamk_f32 v233, v80, 0x3dd53b94, v164
	v_fmac_f32_e32 v164, 0x3dd53b94, v81
	s_waitcnt vmcnt(0) lgkmcnt(0)
	s_barrier
	ds_read_b128 v[214:217], v203
	ds_read_b128 v[222:225], v203 offset:12288
	ds_read_b128 v[236:239], v204
	ds_read_b128 v[240:243], v204 offset:12288
	ds_read_b128 v[66:69], v201 offset:12288
	ds_read_b128 v[70:73], v201
	ds_read_b128 v[244:247], v202
	ds_read_b128 v[176:179], v202 offset:12288
	s_waitcnt lgkmcnt(2)
	v_mfma_f32_32x32x16_bf16 v[82:97], v[70:73], v[128:131], 0
	v_exp_f32_e32 v166, v166
	v_exp_f32_e32 v167, v167
	v_exp_f32_e32 v218, v169
	v_exp_f32_e32 v219, v170
	v_exp_f32_e32 v165, v165
	v_exp_f32_e32 v164, v164
	v_mfma_f32_32x32x16_bf16 v[82:97], v[214:217], v[124:127], v[82:97]
	v_mfma_f32_32x32x16_bf16 v[82:97], v[236:239], v[120:123], v[82:97]
	v_mfma_f32_32x32x16_bf16 v[66:81], v[66:69], v[128:131], 0
	s_waitcnt lgkmcnt(1)
	v_mfma_f32_32x32x16_bf16 v[82:97], v[244:247], v[116:119], v[82:97]
	v_mfma_f32_32x32x16_bf16 v[66:81], v[222:225], v[124:127], v[66:81]
	ds_read_b128 v[214:217], v201 offset:128
	ds_read_b128 v[222:225], v201 offset:12416
	s_waitcnt lgkmcnt(1)
	v_mfma_f32_32x32x16_bf16 v[82:97], v[214:217], v[112:115], v[82:97]
	v_mfma_f32_32x32x16_bf16 v[66:81], v[240:243], v[120:123], v[66:81]
	ds_read_b128 v[236:239], v203 offset:128
	ds_read_b128 v[240:243], v203 offset:12416
	s_waitcnt lgkmcnt(1)
	v_mfma_f32_32x32x16_bf16 v[82:97], v[236:239], v[108:111], v[82:97]
	v_mfma_f32_32x32x16_bf16 v[66:81], v[176:179], v[116:119], v[66:81]
	ds_read_b128 v[176:179], v204 offset:128
	ds_read_b128 v[244:247], v204 offset:12416
	s_waitcnt lgkmcnt(1)
	v_mfma_f32_32x32x16_bf16 v[82:97], v[176:179], v[104:107], v[82:97]
	v_mfma_f32_32x32x16_bf16 v[66:81], v[222:225], v[112:115], v[66:81]
	ds_read_b128 v[214:217], v202 offset:128
	ds_read_b128 v[222:225], v202 offset:12416
	s_waitcnt lgkmcnt(1)
	v_mfma_f32_32x32x16_bf16 v[82:97], v[214:217], v[100:103], v[82:97]
	v_mfma_f32_32x32x16_bf16 v[66:81], v[240:243], v[108:111], v[66:81]
	ds_read_b128 v[236:239], v201 offset:256
	ds_read_b128 v[240:243], v201 offset:12544
	s_waitcnt lgkmcnt(1)
	v_mfma_f32_32x32x16_bf16 v[82:97], v[236:239], v[144:147], v[82:97]
	v_mfma_f32_32x32x16_bf16 v[66:81], v[244:247], v[104:107], v[66:81]
	ds_read_b128 v[176:179], v203 offset:256
	ds_read_b128 v[244:247], v203 offset:12544
	s_waitcnt lgkmcnt(1)
	v_mfma_f32_32x32x16_bf16 v[82:97], v[176:179], v[140:143], v[82:97]
	v_exp_f32_e32 v178, v175
	v_exp_f32_e32 v179, v211
	v_exp_f32_e32 v211, v229
	v_mfma_f32_32x32x16_bf16 v[66:81], v[222:225], v[100:103], v[66:81]
	ds_read_b128 v[214:217], v204 offset:256
	ds_read_b128 v[222:225], v204 offset:12544
	s_waitcnt lgkmcnt(1)
	v_mfma_f32_32x32x16_bf16 v[82:97], v[214:217], v[136:139], v[82:97]
	v_exp_f32_e32 v217, v168
	v_add_f32_e32 v168, 0, v161
	v_add_f32_e32 v168, v163, v168
	v_add_f32_e32 v168, v159, v168
	v_add_f32_e32 v168, v162, v168
	v_add_f32_e32 v168, v158, v168
	v_add_f32_e32 v168, v160, v168
	v_mfma_f32_32x32x16_bf16 v[66:81], v[240:243], v[144:147], v[66:81]
	v_add_f32_e32 v168, v156, v168
	v_add_f32_e32 v168, v157, v168
	v_add_f32_e32 v168, v153, v168
	v_add_f32_e32 v168, v155, v168
	v_add_f32_e32 v168, v152, v168
	v_add_f32_e32 v168, v154, v168
	v_add_f32_e32 v168, v149, v168
	v_mfma_f32_32x32x16_bf16 v[66:81], v[244:247], v[140:143], v[66:81]
	v_add_f32_e32 v168, v151, v168
	v_add_f32_e32 v168, v148, v168
	v_exp_f32_e32 v215, v230
	v_add_f32_e32 v168, v150, v168
	v_exp_f32_e32 v216, v231
	v_add_f32_e32 v168, v178, v168
	v_add_f32_e32 v168, v179, v168
	s_waitcnt lgkmcnt(0)
	v_mfma_f32_32x32x16_bf16 v[66:81], v[222:225], v[136:139], v[66:81]
	v_add_f32_e32 v168, v211, v168
	v_add_f32_e32 v168, v215, v168
	v_add_f32_e32 v168, v216, v168
	ds_read_b128 v[236:239], v202 offset:256
	ds_read_b128 v[240:243], v202 offset:12544
	v_add_f32_e32 v168, v166, v168
	v_exp_f32_e32 v223, v171
	v_add_f32_e32 v168, v167, v168
	v_exp_f32_e32 v224, v174
	v_add_f32_e32 v168, v217, v168
	v_add_f32_e32 v168, v218, v168
	v_exp_f32_e32 v225, v232
	v_add_f32_e32 v168, v219, v168
	s_waitcnt lgkmcnt(1)
	v_mfma_f32_32x32x16_bf16 v[82:97], v[236:239], v[132:135], v[82:97]
	v_exp_f32_e32 v231, v233
	v_add_f32_e32 v168, v223, v168
	v_add_f32_e32 v168, v224, v168
	v_add_f32_e32 v168, v165, v168
	v_add_f32_e32 v168, v225, v168
	v_add_f32_e32 v168, v231, v168
	v_add_f32_e32 v229, v164, v168
	s_waitcnt lgkmcnt(0)
	v_mfma_f32_32x32x16_bf16 v[66:81], v[240:243], v[132:135], v[66:81]
	v_mov_b32_e32 v230, v229
	v_cvt_pk_bf16_f32 v168, v161, v163
	v_cvt_pk_bf16_f32 v169, v159, v162
	v_cvt_pk_bf16_f32 v170, v158, v160
	v_cvt_pk_bf16_f32 v171, v156, v157
	s_nop 1
	v_permlane32_swap_b32_e32 v229, v230
	v_permlane32_swap_b32_e32 v168, v170
	v_permlane32_swap_b32_e32 v169, v171
	v_cvt_pk_bf16_f32 v174, v153, v155
	v_cvt_pk_bf16_f32 v175, v152, v154
	v_cvt_pk_bf16_f32 v176, v149, v151
	v_cvt_pk_bf16_f32 v177, v148, v150
	v_cvt_pk_bf16_f32 v214, v178, v179
	v_cvt_pk_bf16_f32 v215, v211, v215
	v_cvt_pk_bf16_f32 v216, v216, v166
	v_cvt_pk_bf16_f32 v217, v167, v217
	v_cvt_pk_bf16_f32 v222, v218, v219
	v_cvt_pk_bf16_f32 v223, v223, v224
	v_cvt_pk_bf16_f32 v224, v165, v225
	v_cvt_pk_bf16_f32 v225, v231, v164
	s_nop 0
	v_permlane32_swap_b32_e32 v174, v176
	v_permlane32_swap_b32_e32 v175, v177
	v_permlane32_swap_b32_e32 v214, v216
	v_permlane32_swap_b32_e32 v215, v217
	v_permlane32_swap_b32_e32 v222, v224
	v_permlane32_swap_b32_e32 v223, v225
	v_readfirstlane_b32 s4, v0
	s_nop 0
	s_lshl_b32 s5, s4, 4
	s_mul_i32 s4, s5, 3
	s_add_i32 m0, s4, 0xe000
	s_nop 0
	global_load_lds_dwordx4 v[182:183], off
	s_add_i32 m0, s4, 0xe400
	s_nop 0
	global_load_lds_dwordx4 v[184:185], off
	s_add_i32 m0, s4, 0xe800
	s_nop 0
	global_load_lds_dwordx4 v[186:187], off
	s_lshl_b32 s5, s5, 1
	s_mov_b32 m0, s5
	s_nop 0
	global_load_lds_dwordx4 v[206:207], off
	s_add_i32 m0, s5, 0x380
	s_nop 0
	global_load_lds_dwordx4 v[206:207], off offset:128
	v_add_co_u32_e32 v182, vcc, v182, v205
	s_nop 1
	v_addc_co_u32_e32 v183, vcc, 0, v183, vcc
	v_add_co_u32_e32 v184, vcc, v184, v208
	s_nop 1
	v_addc_co_u32_e32 v185, vcc, 0, v185, vcc
	v_add_co_u32_e32 v186, vcc, v186, v209
	s_nop 1
	v_addc_co_u32_e32 v187, vcc, 0, v187, vcc
	v_add_co_u32_e32 v206, vcc, 0x38000, v206
	s_nop 1
	v_addc_co_u32_e32 v207, vcc, 0, v207, vcc
	ds_read_b64_tr_b16 v[188:189], v198 offset:0
	ds_read_b64_tr_b16 v[190:191], v198 offset:0x800
	ds_read_b64_tr_b16 v[236:237], v198 offset:0x1000
	ds_read_b64_tr_b16 v[238:239], v198 offset:0x1800
	ds_read_b64_tr_b16 v[240:241], v198 offset:0x2000
	ds_read_b64_tr_b16 v[242:243], v198 offset:0x2800
	ds_read_b64_tr_b16 v[244:245], v198 offset:0x3000
	ds_read_b64_tr_b16 v[246:247], v198 offset:0x3800
	s_waitcnt lgkmcnt(0)
	s_nop 0
	v_mfma_f32_32x32x16_bf16 v[2:17], v[168:171], v[188:191], v[2:17]
	ds_read_b64_tr_b16 v[188:189], v198 offset:0x200
	ds_read_b64_tr_b16 v[190:191], v198 offset:0xa00
	v_mfma_f32_32x32x16_bf16 v[2:17], v[174:177], v[236:239], v[2:17]
	ds_read_b64_tr_b16 v[236:237], v198 offset:0x1200
	ds_read_b64_tr_b16 v[238:239], v198 offset:0x1a00
	v_mfma_f32_32x32x16_bf16 v[2:17], v[214:217], v[240:243], v[2:17]
	ds_read_b64_tr_b16 v[240:241], v198 offset:0x2200
	ds_read_b64_tr_b16 v[242:243], v198 offset:0x2a00
	v_mfma_f32_32x32x16_bf16 v[2:17], v[222:225], v[244:247], v[2:17]
	ds_read_b64_tr_b16 v[244:245], v198 offset:0x3200
	ds_read_b64_tr_b16 v[246:247], v198 offset:0x3a00
	s_waitcnt lgkmcnt(0)
	v_mfma_f32_32x32x16_bf16 v[50:65], v[168:171], v[188:191], v[50:65]
	ds_read_b64_tr_b16 v[188:189], v198 offset:0x400
	ds_read_b64_tr_b16 v[190:191], v198 offset:0xc00
	v_mfma_f32_32x32x16_bf16 v[50:65], v[174:177], v[236:239], v[50:65]
	ds_read_b64_tr_b16 v[236:237], v198 offset:0x1400
	ds_read_b64_tr_b16 v[238:239], v198 offset:0x1c00
	v_mfma_f32_32x32x16_bf16 v[50:65], v[214:217], v[240:243], v[50:65]
	ds_read_b64_tr_b16 v[240:241], v198 offset:0x2400
	ds_read_b64_tr_b16 v[242:243], v198 offset:0x2c00
	v_mfma_f32_32x32x16_bf16 v[50:65], v[222:225], v[244:247], v[50:65]
	ds_read_b64_tr_b16 v[244:245], v198 offset:0x3400
	ds_read_b64_tr_b16 v[246:247], v198 offset:0x3c00
	s_waitcnt lgkmcnt(0)
	v_mfma_f32_32x32x16_bf16 v[34:49], v[168:171], v[188:191], v[34:49]
	ds_read_b64_tr_b16 v[188:189], v198 offset:0x600
	ds_read_b64_tr_b16 v[190:191], v198 offset:0xe00
	v_mfma_f32_32x32x16_bf16 v[34:49], v[174:177], v[236:239], v[34:49]
	ds_read_b64_tr_b16 v[236:237], v198 offset:0x1600
	ds_read_b64_tr_b16 v[238:239], v198 offset:0x1e00
	v_mfma_f32_32x32x16_bf16 v[34:49], v[214:217], v[240:243], v[34:49]
	ds_read_b64_tr_b16 v[240:241], v198 offset:0x2600
	ds_read_b64_tr_b16 v[242:243], v198 offset:0x2e00
	v_mfma_f32_32x32x16_bf16 v[34:49], v[222:225], v[244:247], v[34:49]
	ds_read_b64_tr_b16 v[244:245], v198 offset:0x3600
	ds_read_b64_tr_b16 v[246:247], v198 offset:0x3e00
	s_waitcnt lgkmcnt(0)
	v_mfma_f32_32x32x16_bf16 v[18:33], v[168:171], v[188:191], v[18:33]
	v_max_f32_e32 v168, v83, v83
	v_max_f32_e32 v169, v82, v82
	v_max_f32_e32 v168, v169, v168
	v_max3_f32 v168, v168, v84, v85
	v_max3_f32 v168, v168, v86, v87
	v_max3_f32 v168, v168, v88, v89
	v_max3_f32 v168, v168, v90, v91
	v_max3_f32 v168, v168, v92, v93
	v_max3_f32 v168, v168, v94, v95
	v_mfma_f32_32x32x16_bf16 v[18:33], v[174:177], v[236:239], v[18:33]
	v_max3_f32 v168, v168, v96, v97
	v_max3_f32 v168, v168, v66, v67
	v_max3_f32 v168, v168, v68, v69
	v_max3_f32 v168, v168, v70, v71
	v_max3_f32 v168, v168, v72, v73
	v_max3_f32 v168, v168, v74, v75
	v_max3_f32 v168, v168, v76, v77
	v_max3_f32 v168, v168, v78, v79
	v_mfma_f32_32x32x16_bf16 v[18:33], v[214:217], v[240:243], v[18:33]
	v_max3_f32 v168, v168, v80, v81
	v_mov_b32_e32 v169, v168
	s_nop 1
	v_permlane32_swap_b32_e32 v168, v169
	v_max_f32_e32 v169, v169, v169
	v_max_f32_e32 v168, v168, v168
	v_max_f32_e32 v168, v168, v169
	v_sub_f32_e32 v169, v168, v173
	v_cmp_ge_f32_e32 vcc, s11, v169
	v_max_f32_e32 v169, v173, v173
	v_max_f32_e32 v169, v169, v168
	v_mfma_f32_32x32x16_bf16 v[18:33], v[222:225], v[244:247], v[18:33]
	v_sub_f32_e32 v168, v173, v169
	v_mul_f32_e32 v168, 0x3dd53b94, v168
	v_exp_f32_e32 v168, v168
	s_cmp_eq_u64 vcc, exec
	s_cselect_b64 s[18:19], -1, 0
	v_cndmask_b32_e64 v168, v168, 1.0, s[18:19]
	v_cmp_gt_f32_e32 vcc, 1.0, v168
	s_cbranch_vccz .LBB0_1353
	s_mov_b64 s[4:5], exec
	s_and_b64 s[22:23], s[4:5], s[0:1]
	v_mov_b32_e32 v246, v227
	s_mov_b64 exec, s[22:23]
	ds_write_b32 v197, v168 offset:128
	s_or_b64 exec, exec, s[4:5]
	s_waitcnt lgkmcnt(0)
	v_add_u32_e32 v160, v196, v98
	ds_read_b128 v[148:151], v160 offset:224
	ds_read_b128 v[152:155], v160 offset:192
	ds_read_b128 v[156:159], v160 offset:160
	ds_read_b128 v[160:163], v160 offset:128
	s_waitcnt lgkmcnt(3)
	v_pk_mul_f32 v[14:15], v[14:15], v[148:149]
	s_waitcnt lgkmcnt(2)
	v_pk_mul_f32 v[10:11], v[10:11], v[152:153]
	s_waitcnt lgkmcnt(1)
	v_pk_mul_f32 v[6:7], v[6:7], v[156:157]
	v_pk_mul_f32 v[16:17], v[16:17], v[150:151]
	v_pk_mul_f32 v[12:13], v[12:13], v[154:155]
	v_pk_mul_f32 v[8:9], v[8:9], v[158:159]
	s_waitcnt lgkmcnt(0)
	v_pk_mul_f32 v[4:5], v[4:5], v[162:163]
	v_pk_mul_f32 v[2:3], v[2:3], v[160:161]
	v_pk_mul_f32 v[62:63], v[62:63], v[148:149]
	v_pk_mul_f32 v[58:59], v[58:59], v[152:153]
	v_pk_mul_f32 v[54:55], v[54:55], v[156:157]
	v_pk_mul_f32 v[64:65], v[64:65], v[150:151]
	v_pk_mul_f32 v[60:61], v[60:61], v[154:155]
	v_pk_mul_f32 v[56:57], v[56:57], v[158:159]
	v_pk_mul_f32 v[52:53], v[52:53], v[162:163]
	v_pk_mul_f32 v[50:51], v[50:51], v[160:161]
	v_pk_mul_f32 v[46:47], v[46:47], v[148:149]
	v_pk_mul_f32 v[42:43], v[42:43], v[152:153]
	v_pk_mul_f32 v[38:39], v[38:39], v[156:157]
	v_pk_mul_f32 v[48:49], v[48:49], v[150:151]
	v_pk_mul_f32 v[44:45], v[44:45], v[154:155]
	v_pk_mul_f32 v[40:41], v[40:41], v[158:159]
	v_pk_mul_f32 v[36:37], v[36:37], v[162:163]
	v_pk_mul_f32 v[34:35], v[34:35], v[160:161]
	v_pk_mul_f32 v[30:31], v[30:31], v[148:149]
	v_pk_mul_f32 v[26:27], v[26:27], v[152:153]
	v_pk_mul_f32 v[22:23], v[22:23], v[156:157]
	v_pk_mul_f32 v[32:33], v[32:33], v[150:151]
	v_pk_mul_f32 v[28:29], v[28:29], v[154:155]
	v_pk_mul_f32 v[24:25], v[24:25], v[158:159]
	v_pk_mul_f32 v[20:21], v[20:21], v[162:163]
	v_pk_mul_f32 v[18:19], v[18:19], v[160:161]
	s_branch .LBB0_1354
